# v28_g2
# speedup vs baseline: 1.0544x; 1.0122x over previous
.LBB3_169:
	s_cmp_lt_u32 s12, 64
	s_cbranch_scc1 .Lmy_l1_main
	s_cmp_lg_u32 s12, 64
	s_cbranch_scc1 .LBB3_168
	v_mov_b32_e32 v164, v122
	s_waitcnt vmcnt(15)
	v_mfma_f32_16x16x32_f16 v[132:135], v[2:5], v[124:127], v[98:101]
	v_mfma_f32_16x16x32_f16 v[136:139], v[10:13], v[124:127], v[98:101]
	v_mfma_f32_16x16x32_f16 v[140:143], v[18:21], v[124:127], v[98:101]
	v_mfma_f32_16x16x32_f16 v[144:147], v[26:29], v[124:127], v[98:101]
	v_mfma_f32_16x16x32_f16 v[132:135], v[6:9], v[128:131], v[132:135]
	s_nop 1
	v_mfma_f32_16x16x32_f16 v[136:139], v[14:17], v[128:131], v[136:139]
	s_nop 1
	v_mfma_f32_16x16x32_f16 v[140:143], v[22:25], v[128:131], v[140:143]
	s_nop 1
	v_mfma_f32_16x16x32_f16 v[144:147], v[30:33], v[128:131], v[144:147]
	s_nop 1
	v_cndmask_b32_e64 v160, v136, v132, s[0:1]
	v_cndmask_b32_e64 v161, v137, v133, s[0:1]
	v_cndmask_b32_e64 v162, v138, v134, s[0:1]
	v_cndmask_b32_e64 v163, v139, v135, s[0:1]
	v_cndmask_b32_e64 v160, v140, v160, s[2:3]
	v_cndmask_b32_e64 v161, v141, v161, s[2:3]
	v_cndmask_b32_e64 v162, v142, v162, s[2:3]
	v_cndmask_b32_e64 v163, v143, v163, s[2:3]
	v_cndmask_b32_e64 v156, v160, v144, s[4:5]
	v_cndmask_b32_e64 v157, v161, v145, s[4:5]
	v_exp_f32_e32 v156, v156
	v_exp_f32_e32 v157, v157
	v_cndmask_b32_e64 v158, v162, v146, s[4:5]
	v_cndmask_b32_e64 v159, v163, v147, s[4:5]
	v_pk_add_f32 v[156:157], v[156:157], 1.0 op_sel_hi:[1,0]
	v_exp_f32_e32 v158, v158
	v_rcp_f32_e32 v156, v156
	v_rcp_f32_e32 v157, v157
	v_exp_f32_e32 v159, v159
	v_pk_fma_f32 v[148:149], v[110:111], v[156:157], v[152:153]
	v_pk_add_f32 v[158:159], v[158:159], 1.0 op_sel_hi:[1,0]
	v_cvt_pk_f16_f32 v124, v148, v149
	v_rcp_f32_e32 v158, v158
	v_rcp_f32_e32 v159, v159
	v_mov_b32_dpp v125, v124 quad_perm:[1,2,3,0] row_mask:0xf bank_mask:0xf bound_ctrl:1
	v_mov_b32_dpp v126, v124 quad_perm:[2,3,0,1] row_mask:0xf bank_mask:0xf bound_ctrl:1
	v_mov_b32_dpp v127, v124 quad_perm:[3,0,1,2] row_mask:0xf bank_mask:0xf bound_ctrl:1
	v_pk_fma_f32 v[150:151], v[112:113], v[158:159], v[154:155]
	s_nop 0
	v_cvt_pk_f16_f32 v128, v150, v151
	ds_write_b32 v164, v124 offset:0
	v_fma_f32 v152, v102, v148, v104
	v_mov_b32_dpp v129, v128 quad_perm:[1,2,3,0] row_mask:0xf bank_mask:0xf bound_ctrl:1
	v_mov_b32_dpp v130, v128 quad_perm:[2,3,0,1] row_mask:0xf bank_mask:0xf bound_ctrl:1
	v_mov_b32_dpp v131, v128 quad_perm:[3,0,1,2] row_mask:0xf bank_mask:0xf bound_ctrl:1
	ds_write_b32 v164, v128 offset:4
	v_fma_f32 v153, v103, v149, v105
	v_fma_f32 v154, v106, v150, v108
	v_fma_f32 v155, v107, v151, v109
	s_branch .LBB3_168
.Lmy_l1_main:
	s_bitcmp1_b32 s12, 0
	s_cselect_b32 s10, 0x2100, 0
	s_nop 0
	v_add_u32_e32 v164, s10, v122
	s_waitcnt vmcnt(15)
	v_mfma_f32_16x16x32_f16 v[132:135], v[2:5], v[124:127], v[98:101]
	v_mfma_f32_16x16x32_f16 v[136:139], v[10:13], v[124:127], v[98:101]
	v_mfma_f32_16x16x32_f16 v[140:143], v[18:21], v[124:127], v[98:101]
	v_mfma_f32_16x16x32_f16 v[144:147], v[26:29], v[124:127], v[98:101]
	v_mfma_f32_16x16x32_f16 v[132:135], v[6:9], v[128:131], v[132:135]
	s_nop 1
	v_mfma_f32_16x16x32_f16 v[136:139], v[14:17], v[128:131], v[136:139]
	s_nop 1
	v_mfma_f32_16x16x32_f16 v[140:143], v[22:25], v[128:131], v[140:143]
	s_nop 1
	v_mfma_f32_16x16x32_f16 v[144:147], v[30:33], v[128:131], v[144:147]
	global_load_dwordx4 v[98:101], v[0:1], off offset:-2048
	s_nop 0
	v_cndmask_b32_e64 v160, v136, v132, s[0:1]
	v_cndmask_b32_e64 v161, v137, v133, s[0:1]
	v_cndmask_b32_e64 v162, v138, v134, s[0:1]
	v_cndmask_b32_e64 v163, v139, v135, s[0:1]
	v_cndmask_b32_e64 v160, v140, v160, s[2:3]
	v_cndmask_b32_e64 v161, v141, v161, s[2:3]
	v_cndmask_b32_e64 v162, v142, v162, s[2:3]
	v_cndmask_b32_e64 v163, v143, v163, s[2:3]
	v_cndmask_b32_e64 v156, v160, v144, s[4:5]
	v_cndmask_b32_e64 v157, v161, v145, s[4:5]
	v_exp_f32_e32 v156, v156
	v_exp_f32_e32 v157, v157
	v_cndmask_b32_e64 v158, v162, v146, s[4:5]
	v_cndmask_b32_e64 v159, v163, v147, s[4:5]
	v_pk_add_f32 v[156:157], v[156:157], 1.0 op_sel_hi:[1,0]
	v_exp_f32_e32 v158, v158
	v_rcp_f32_e32 v156, v156
	v_rcp_f32_e32 v157, v157
	v_exp_f32_e32 v159, v159
	v_pk_fma_f32 v[148:149], v[110:111], v[156:157], v[152:153]
	v_pk_add_f32 v[158:159], v[158:159], 1.0 op_sel_hi:[1,0]
	v_cvt_pk_f16_f32 v124, v148, v149
	v_rcp_f32_e32 v158, v158
	v_rcp_f32_e32 v159, v159
	v_mov_b32_dpp v125, v124 quad_perm:[1,2,3,0] row_mask:0xf bank_mask:0xf bound_ctrl:1
	v_mov_b32_dpp v126, v124 quad_perm:[2,3,0,1] row_mask:0xf bank_mask:0xf bound_ctrl:1
	v_mov_b32_dpp v127, v124 quad_perm:[3,0,1,2] row_mask:0xf bank_mask:0xf bound_ctrl:1
	v_pk_fma_f32 v[150:151], v[112:113], v[158:159], v[154:155]
	s_waitcnt vmcnt(15)
	v_mfma_f32_16x16x32_f16 v[132:135], v[2:5], v[124:127], v[70:73]
	v_cvt_pk_f16_f32 v128, v150, v151
	s_nop 0
	v_mfma_f32_16x16x32_f16 v[136:139], v[10:13], v[124:127], v[70:73]
	v_mov_b32_dpp v129, v128 quad_perm:[1,2,3,0] row_mask:0xf bank_mask:0xf bound_ctrl:1
	v_mov_b32_dpp v130, v128 quad_perm:[2,3,0,1] row_mask:0xf bank_mask:0xf bound_ctrl:1
	v_mfma_f32_16x16x32_f16 v[140:143], v[18:21], v[124:127], v[70:73]
	v_mov_b32_dpp v131, v128 quad_perm:[3,0,1,2] row_mask:0xf bank_mask:0xf bound_ctrl:1
	s_nop 0
	v_mfma_f32_16x16x32_f16 v[144:147], v[26:29], v[124:127], v[70:73]
	v_mfma_f32_16x16x32_f16 v[132:135], v[6:9], v[128:131], v[132:135]
	v_fma_f32 v154, v106, v150, v108
	v_fma_f32 v155, v107, v151, v109
	v_mfma_f32_16x16x32_f16 v[136:139], v[14:17], v[128:131], v[136:139]
	v_fma_f32 v152, v102, v148, v104
	v_fma_f32 v153, v103, v149, v105
	v_mfma_f32_16x16x32_f16 v[140:143], v[22:25], v[128:131], v[140:143]
	ds_write_b32 v164, v124 offset:0
	ds_write_b32 v164, v128 offset:4
	v_mfma_f32_16x16x32_f16 v[144:147], v[30:33], v[128:131], v[144:147]
	global_load_dwordx4 v[70:73], v[0:1], off offset:-1792
	s_nop 0
	v_cndmask_b32_e64 v160, v136, v132, s[0:1]
	v_cndmask_b32_e64 v161, v137, v133, s[0:1]
	v_cndmask_b32_e64 v162, v138, v134, s[0:1]
	v_cndmask_b32_e64 v163, v139, v135, s[0:1]
	v_cndmask_b32_e64 v160, v140, v160, s[2:3]
	v_cndmask_b32_e64 v161, v141, v161, s[2:3]
	v_cndmask_b32_e64 v162, v142, v162, s[2:3]
	v_cndmask_b32_e64 v163, v143, v163, s[2:3]
	v_cndmask_b32_e64 v156, v160, v144, s[4:5]
	v_cndmask_b32_e64 v157, v161, v145, s[4:5]
	v_exp_f32_e32 v156, v156
	v_exp_f32_e32 v157, v157
	v_cndmask_b32_e64 v158, v162, v146, s[4:5]
	v_cndmask_b32_e64 v159, v163, v147, s[4:5]
	v_pk_add_f32 v[156:157], v[156:157], 1.0 op_sel_hi:[1,0]
	v_exp_f32_e32 v158, v158
	v_rcp_f32_e32 v156, v156
	v_rcp_f32_e32 v157, v157
	v_exp_f32_e32 v159, v159
	v_pk_fma_f32 v[148:149], v[110:111], v[156:157], v[152:153]
	v_pk_add_f32 v[158:159], v[158:159], 1.0 op_sel_hi:[1,0]
	v_cvt_pk_f16_f32 v124, v148, v149
	v_rcp_f32_e32 v158, v158
	v_rcp_f32_e32 v159, v159
	v_mov_b32_dpp v125, v124 quad_perm:[1,2,3,0] row_mask:0xf bank_mask:0xf bound_ctrl:1
	v_mov_b32_dpp v126, v124 quad_perm:[2,3,0,1] row_mask:0xf bank_mask:0xf bound_ctrl:1
	v_mov_b32_dpp v127, v124 quad_perm:[3,0,1,2] row_mask:0xf bank_mask:0xf bound_ctrl:1
	v_pk_fma_f32 v[150:151], v[112:113], v[158:159], v[154:155]
	s_waitcnt vmcnt(15)
	v_mfma_f32_16x16x32_f16 v[132:135], v[2:5], v[124:127], v[78:81]
	v_cvt_pk_f16_f32 v128, v150, v151
	s_nop 0
	v_mfma_f32_16x16x32_f16 v[136:139], v[10:13], v[124:127], v[78:81]
	v_mov_b32_dpp v129, v128 quad_perm:[1,2,3,0] row_mask:0xf bank_mask:0xf bound_ctrl:1
	v_mov_b32_dpp v130, v128 quad_perm:[2,3,0,1] row_mask:0xf bank_mask:0xf bound_ctrl:1
	v_mfma_f32_16x16x32_f16 v[140:143], v[18:21], v[124:127], v[78:81]
	v_mov_b32_dpp v131, v128 quad_perm:[3,0,1,2] row_mask:0xf bank_mask:0xf bound_ctrl:1
	s_nop 0
	v_mfma_f32_16x16x32_f16 v[144:147], v[26:29], v[124:127], v[78:81]
	v_mfma_f32_16x16x32_f16 v[132:135], v[6:9], v[128:131], v[132:135]
	v_fma_f32 v154, v106, v150, v108
	v_fma_f32 v155, v107, v151, v109
	v_mfma_f32_16x16x32_f16 v[136:139], v[14:17], v[128:131], v[136:139]
	v_fma_f32 v152, v102, v148, v104
	v_fma_f32 v153, v103, v149, v105
	v_mfma_f32_16x16x32_f16 v[140:143], v[22:25], v[128:131], v[140:143]
	ds_write_b32 v164, v124 offset:528
	ds_write_b32 v164, v128 offset:532
	v_mfma_f32_16x16x32_f16 v[144:147], v[30:33], v[128:131], v[144:147]
	global_load_dwordx4 v[78:81], v[0:1], off offset:-1536
	s_nop 0
	v_cndmask_b32_e64 v160, v136, v132, s[0:1]
	v_cndmask_b32_e64 v161, v137, v133, s[0:1]
	v_cndmask_b32_e64 v162, v138, v134, s[0:1]
	v_cndmask_b32_e64 v163, v139, v135, s[0:1]
	v_cndmask_b32_e64 v160, v140, v160, s[2:3]
	v_cndmask_b32_e64 v161, v141, v161, s[2:3]
	v_cndmask_b32_e64 v162, v142, v162, s[2:3]
	v_cndmask_b32_e64 v163, v143, v163, s[2:3]
	v_cndmask_b32_e64 v156, v160, v144, s[4:5]
	v_cndmask_b32_e64 v157, v161, v145, s[4:5]
	v_exp_f32_e32 v156, v156
	v_exp_f32_e32 v157, v157
	v_cndmask_b32_e64 v158, v162, v146, s[4:5]
	v_cndmask_b32_e64 v159, v163, v147, s[4:5]
	v_pk_add_f32 v[156:157], v[156:157], 1.0 op_sel_hi:[1,0]
	v_exp_f32_e32 v158, v158
	v_rcp_f32_e32 v156, v156
	v_rcp_f32_e32 v157, v157
	v_exp_f32_e32 v159, v159
	v_pk_fma_f32 v[148:149], v[110:111], v[156:157], v[152:153]
	v_pk_add_f32 v[158:159], v[158:159], 1.0 op_sel_hi:[1,0]
	v_cvt_pk_f16_f32 v124, v148, v149
	v_rcp_f32_e32 v158, v158
	v_rcp_f32_e32 v159, v159
	v_mov_b32_dpp v125, v124 quad_perm:[1,2,3,0] row_mask:0xf bank_mask:0xf bound_ctrl:1
	v_mov_b32_dpp v126, v124 quad_perm:[2,3,0,1] row_mask:0xf bank_mask:0xf bound_ctrl:1
	v_mov_b32_dpp v127, v124 quad_perm:[3,0,1,2] row_mask:0xf bank_mask:0xf bound_ctrl:1
	v_pk_fma_f32 v[150:151], v[112:113], v[158:159], v[154:155]
	s_waitcnt vmcnt(15)
	v_mfma_f32_16x16x32_f16 v[132:135], v[2:5], v[124:127], v[86:89]
	v_cvt_pk_f16_f32 v128, v150, v151
	s_nop 0
	v_mfma_f32_16x16x32_f16 v[136:139], v[10:13], v[124:127], v[86:89]
	v_mov_b32_dpp v129, v128 quad_perm:[1,2,3,0] row_mask:0xf bank_mask:0xf bound_ctrl:1
	v_mov_b32_dpp v130, v128 quad_perm:[2,3,0,1] row_mask:0xf bank_mask:0xf bound_ctrl:1
	v_mfma_f32_16x16x32_f16 v[140:143], v[18:21], v[124:127], v[86:89]
	v_mov_b32_dpp v131, v128 quad_perm:[3,0,1,2] row_mask:0xf bank_mask:0xf bound_ctrl:1
	s_nop 0
	v_mfma_f32_16x16x32_f16 v[144:147], v[26:29], v[124:127], v[86:89]
	v_mfma_f32_16x16x32_f16 v[132:135], v[6:9], v[128:131], v[132:135]
	v_fma_f32 v154, v106, v150, v108
	v_fma_f32 v155, v107, v151, v109
	v_mfma_f32_16x16x32_f16 v[136:139], v[14:17], v[128:131], v[136:139]
	v_fma_f32 v152, v102, v148, v104
	v_fma_f32 v153, v103, v149, v105
	v_mfma_f32_16x16x32_f16 v[140:143], v[22:25], v[128:131], v[140:143]
	ds_write_b32 v164, v124 offset:1056
	ds_write_b32 v164, v128 offset:1060
	v_mfma_f32_16x16x32_f16 v[144:147], v[30:33], v[128:131], v[144:147]
	global_load_dwordx4 v[86:89], v[0:1], off offset:-1280
	s_nop 0
	v_cndmask_b32_e64 v160, v136, v132, s[0:1]
	v_cndmask_b32_e64 v161, v137, v133, s[0:1]
	v_cndmask_b32_e64 v162, v138, v134, s[0:1]
	v_cndmask_b32_e64 v163, v139, v135, s[0:1]
	v_cndmask_b32_e64 v160, v140, v160, s[2:3]
	v_cndmask_b32_e64 v161, v141, v161, s[2:3]
	v_cndmask_b32_e64 v162, v142, v162, s[2:3]
	v_cndmask_b32_e64 v163, v143, v163, s[2:3]
	v_cndmask_b32_e64 v156, v160, v144, s[4:5]
	v_cndmask_b32_e64 v157, v161, v145, s[4:5]
	v_exp_f32_e32 v156, v156
	v_exp_f32_e32 v157, v157
	v_cndmask_b32_e64 v158, v162, v146, s[4:5]
	v_cndmask_b32_e64 v159, v163, v147, s[4:5]
	v_pk_add_f32 v[156:157], v[156:157], 1.0 op_sel_hi:[1,0]
	v_exp_f32_e32 v158, v158
	v_rcp_f32_e32 v156, v156
	v_rcp_f32_e32 v157, v157
	v_exp_f32_e32 v159, v159
	v_pk_fma_f32 v[148:149], v[110:111], v[156:157], v[152:153]
	v_pk_add_f32 v[158:159], v[158:159], 1.0 op_sel_hi:[1,0]
	v_cvt_pk_f16_f32 v124, v148, v149
	v_rcp_f32_e32 v158, v158
	v_rcp_f32_e32 v159, v159
	v_mov_b32_dpp v125, v124 quad_perm:[1,2,3,0] row_mask:0xf bank_mask:0xf bound_ctrl:1
	v_mov_b32_dpp v126, v124 quad_perm:[2,3,0,1] row_mask:0xf bank_mask:0xf bound_ctrl:1
	v_mov_b32_dpp v127, v124 quad_perm:[3,0,1,2] row_mask:0xf bank_mask:0xf bound_ctrl:1
	v_pk_fma_f32 v[150:151], v[112:113], v[158:159], v[154:155]
	s_waitcnt vmcnt(15)
	v_mfma_f32_16x16x32_f16 v[132:135], v[2:5], v[124:127], v[94:97]
	v_cvt_pk_f16_f32 v128, v150, v151
	s_nop 0
	v_mfma_f32_16x16x32_f16 v[136:139], v[10:13], v[124:127], v[94:97]
	v_mov_b32_dpp v129, v128 quad_perm:[1,2,3,0] row_mask:0xf bank_mask:0xf bound_ctrl:1
	v_mov_b32_dpp v130, v128 quad_perm:[2,3,0,1] row_mask:0xf bank_mask:0xf bound_ctrl:1
	v_mfma_f32_16x16x32_f16 v[140:143], v[18:21], v[124:127], v[94:97]
	v_mov_b32_dpp v131, v128 quad_perm:[3,0,1,2] row_mask:0xf bank_mask:0xf bound_ctrl:1
	s_nop 0
	v_mfma_f32_16x16x32_f16 v[144:147], v[26:29], v[124:127], v[94:97]
	v_mfma_f32_16x16x32_f16 v[132:135], v[6:9], v[128:131], v[132:135]
	v_fma_f32 v154, v106, v150, v108
	v_fma_f32 v155, v107, v151, v109
	v_mfma_f32_16x16x32_f16 v[136:139], v[14:17], v[128:131], v[136:139]
	v_fma_f32 v152, v102, v148, v104
	v_fma_f32 v153, v103, v149, v105
	v_mfma_f32_16x16x32_f16 v[140:143], v[22:25], v[128:131], v[140:143]
	ds_write_b32 v164, v124 offset:1584
	ds_write_b32 v164, v128 offset:1588
	v_mfma_f32_16x16x32_f16 v[144:147], v[30:33], v[128:131], v[144:147]
	global_load_dwordx4 v[94:97], v[0:1], off offset:-1024
	s_nop 0
	v_cndmask_b32_e64 v160, v136, v132, s[0:1]
	v_cndmask_b32_e64 v161, v137, v133, s[0:1]
	v_cndmask_b32_e64 v162, v138, v134, s[0:1]
	v_cndmask_b32_e64 v163, v139, v135, s[0:1]
	v_cndmask_b32_e64 v160, v140, v160, s[2:3]
	v_cndmask_b32_e64 v161, v141, v161, s[2:3]
	v_cndmask_b32_e64 v162, v142, v162, s[2:3]
	v_cndmask_b32_e64 v163, v143, v163, s[2:3]
	v_cndmask_b32_e64 v156, v160, v144, s[4:5]
	v_cndmask_b32_e64 v157, v161, v145, s[4:5]
	v_exp_f32_e32 v156, v156
	v_exp_f32_e32 v157, v157
	v_cndmask_b32_e64 v158, v162, v146, s[4:5]
	v_cndmask_b32_e64 v159, v163, v147, s[4:5]
	v_pk_add_f32 v[156:157], v[156:157], 1.0 op_sel_hi:[1,0]
	v_exp_f32_e32 v158, v158
	v_rcp_f32_e32 v156, v156
	v_rcp_f32_e32 v157, v157
	v_exp_f32_e32 v159, v159
	v_pk_fma_f32 v[148:149], v[110:111], v[156:157], v[152:153]
	v_pk_add_f32 v[158:159], v[158:159], 1.0 op_sel_hi:[1,0]
	v_cvt_pk_f16_f32 v124, v148, v149
	v_rcp_f32_e32 v158, v158
	v_rcp_f32_e32 v159, v159
	v_mov_b32_dpp v125, v124 quad_perm:[1,2,3,0] row_mask:0xf bank_mask:0xf bound_ctrl:1
	v_mov_b32_dpp v126, v124 quad_perm:[2,3,0,1] row_mask:0xf bank_mask:0xf bound_ctrl:1
	v_mov_b32_dpp v127, v124 quad_perm:[3,0,1,2] row_mask:0xf bank_mask:0xf bound_ctrl:1
	v_pk_fma_f32 v[150:151], v[112:113], v[158:159], v[154:155]
	s_waitcnt vmcnt(15)
	v_mfma_f32_16x16x32_f16 v[132:135], v[2:5], v[124:127], v[90:93]
	v_cvt_pk_f16_f32 v128, v150, v151
	s_nop 0
	v_mfma_f32_16x16x32_f16 v[136:139], v[10:13], v[124:127], v[90:93]
	v_mov_b32_dpp v129, v128 quad_perm:[1,2,3,0] row_mask:0xf bank_mask:0xf bound_ctrl:1
	v_mov_b32_dpp v130, v128 quad_perm:[2,3,0,1] row_mask:0xf bank_mask:0xf bound_ctrl:1
	v_mfma_f32_16x16x32_f16 v[140:143], v[18:21], v[124:127], v[90:93]
	v_mov_b32_dpp v131, v128 quad_perm:[3,0,1,2] row_mask:0xf bank_mask:0xf bound_ctrl:1
	s_nop 0
	v_mfma_f32_16x16x32_f16 v[144:147], v[26:29], v[124:127], v[90:93]
	v_mfma_f32_16x16x32_f16 v[132:135], v[6:9], v[128:131], v[132:135]
	v_fma_f32 v154, v106, v150, v108
	v_fma_f32 v155, v107, v151, v109
	v_mfma_f32_16x16x32_f16 v[136:139], v[14:17], v[128:131], v[136:139]
	v_fma_f32 v152, v102, v148, v104
	v_fma_f32 v153, v103, v149, v105
	v_mfma_f32_16x16x32_f16 v[140:143], v[22:25], v[128:131], v[140:143]
	ds_write_b32 v164, v124 offset:2112
	ds_write_b32 v164, v128 offset:2116
	v_mfma_f32_16x16x32_f16 v[144:147], v[30:33], v[128:131], v[144:147]
	global_load_dwordx4 v[90:93], v[0:1], off offset:-768
	s_nop 0
	v_cndmask_b32_e64 v160, v136, v132, s[0:1]
	v_cndmask_b32_e64 v161, v137, v133, s[0:1]
	v_cndmask_b32_e64 v162, v138, v134, s[0:1]
	v_cndmask_b32_e64 v163, v139, v135, s[0:1]
	v_cndmask_b32_e64 v160, v140, v160, s[2:3]
	v_cndmask_b32_e64 v161, v141, v161, s[2:3]
	v_cndmask_b32_e64 v162, v142, v162, s[2:3]
	v_cndmask_b32_e64 v163, v143, v163, s[2:3]
	v_cndmask_b32_e64 v156, v160, v144, s[4:5]
	v_cndmask_b32_e64 v157, v161, v145, s[4:5]
	v_exp_f32_e32 v156, v156
	v_exp_f32_e32 v157, v157
	v_cndmask_b32_e64 v158, v162, v146, s[4:5]
	v_cndmask_b32_e64 v159, v163, v147, s[4:5]
	v_pk_add_f32 v[156:157], v[156:157], 1.0 op_sel_hi:[1,0]
	v_exp_f32_e32 v158, v158
	v_rcp_f32_e32 v156, v156
	v_rcp_f32_e32 v157, v157
	v_exp_f32_e32 v159, v159
	v_pk_fma_f32 v[148:149], v[110:111], v[156:157], v[152:153]
	v_pk_add_f32 v[158:159], v[158:159], 1.0 op_sel_hi:[1,0]
	v_cvt_pk_f16_f32 v124, v148, v149
	v_rcp_f32_e32 v158, v158
	v_rcp_f32_e32 v159, v159
	v_mov_b32_dpp v125, v124 quad_perm:[1,2,3,0] row_mask:0xf bank_mask:0xf bound_ctrl:1
	v_mov_b32_dpp v126, v124 quad_perm:[2,3,0,1] row_mask:0xf bank_mask:0xf bound_ctrl:1
	v_mov_b32_dpp v127, v124 quad_perm:[3,0,1,2] row_mask:0xf bank_mask:0xf bound_ctrl:1
	v_pk_fma_f32 v[150:151], v[112:113], v[158:159], v[154:155]
	s_waitcnt vmcnt(15)
	v_mfma_f32_16x16x32_f16 v[132:135], v[2:5], v[124:127], v[82:85]
	v_cvt_pk_f16_f32 v128, v150, v151
	s_nop 0
	v_mfma_f32_16x16x32_f16 v[136:139], v[10:13], v[124:127], v[82:85]
	v_mov_b32_dpp v129, v128 quad_perm:[1,2,3,0] row_mask:0xf bank_mask:0xf bound_ctrl:1
	v_mov_b32_dpp v130, v128 quad_perm:[2,3,0,1] row_mask:0xf bank_mask:0xf bound_ctrl:1
	v_mfma_f32_16x16x32_f16 v[140:143], v[18:21], v[124:127], v[82:85]
	v_mov_b32_dpp v131, v128 quad_perm:[3,0,1,2] row_mask:0xf bank_mask:0xf bound_ctrl:1
	s_nop 0
	v_mfma_f32_16x16x32_f16 v[144:147], v[26:29], v[124:127], v[82:85]
	v_mfma_f32_16x16x32_f16 v[132:135], v[6:9], v[128:131], v[132:135]
	v_fma_f32 v154, v106, v150, v108
	v_fma_f32 v155, v107, v151, v109
	v_mfma_f32_16x16x32_f16 v[136:139], v[14:17], v[128:131], v[136:139]
	v_fma_f32 v152, v102, v148, v104
	v_fma_f32 v153, v103, v149, v105
	v_mfma_f32_16x16x32_f16 v[140:143], v[22:25], v[128:131], v[140:143]
	ds_write_b32 v164, v124 offset:2640
	ds_write_b32 v164, v128 offset:2644
	v_mfma_f32_16x16x32_f16 v[144:147], v[30:33], v[128:131], v[144:147]
	global_load_dwordx4 v[82:85], v[0:1], off offset:-512
	s_nop 0
	v_cndmask_b32_e64 v160, v136, v132, s[0:1]
	v_cndmask_b32_e64 v161, v137, v133, s[0:1]
	v_cndmask_b32_e64 v162, v138, v134, s[0:1]
	v_cndmask_b32_e64 v163, v139, v135, s[0:1]
	v_cndmask_b32_e64 v160, v140, v160, s[2:3]
	v_cndmask_b32_e64 v161, v141, v161, s[2:3]
	v_cndmask_b32_e64 v162, v142, v162, s[2:3]
	v_cndmask_b32_e64 v163, v143, v163, s[2:3]
	v_cndmask_b32_e64 v156, v160, v144, s[4:5]
	v_cndmask_b32_e64 v157, v161, v145, s[4:5]
	v_exp_f32_e32 v156, v156
	v_exp_f32_e32 v157, v157
	v_cndmask_b32_e64 v158, v162, v146, s[4:5]
	v_cndmask_b32_e64 v159, v163, v147, s[4:5]
	v_pk_add_f32 v[156:157], v[156:157], 1.0 op_sel_hi:[1,0]
	v_exp_f32_e32 v158, v158
	v_rcp_f32_e32 v156, v156
	v_rcp_f32_e32 v157, v157
	v_exp_f32_e32 v159, v159
	v_pk_fma_f32 v[148:149], v[110:111], v[156:157], v[152:153]
	v_pk_add_f32 v[158:159], v[158:159], 1.0 op_sel_hi:[1,0]
	v_cvt_pk_f16_f32 v124, v148, v149
	v_rcp_f32_e32 v158, v158
	v_rcp_f32_e32 v159, v159
	v_mov_b32_dpp v125, v124 quad_perm:[1,2,3,0] row_mask:0xf bank_mask:0xf bound_ctrl:1
	v_mov_b32_dpp v126, v124 quad_perm:[2,3,0,1] row_mask:0xf bank_mask:0xf bound_ctrl:1
	v_mov_b32_dpp v127, v124 quad_perm:[3,0,1,2] row_mask:0xf bank_mask:0xf bound_ctrl:1
	v_pk_fma_f32 v[150:151], v[112:113], v[158:159], v[154:155]
	s_waitcnt vmcnt(15)
	v_mfma_f32_16x16x32_f16 v[132:135], v[2:5], v[124:127], v[74:77]
	v_cvt_pk_f16_f32 v128, v150, v151
	s_nop 0
	v_mfma_f32_16x16x32_f16 v[136:139], v[10:13], v[124:127], v[74:77]
	v_mov_b32_dpp v129, v128 quad_perm:[1,2,3,0] row_mask:0xf bank_mask:0xf bound_ctrl:1
	v_mov_b32_dpp v130, v128 quad_perm:[2,3,0,1] row_mask:0xf bank_mask:0xf bound_ctrl:1
	v_mfma_f32_16x16x32_f16 v[140:143], v[18:21], v[124:127], v[74:77]
	v_mov_b32_dpp v131, v128 quad_perm:[3,0,1,2] row_mask:0xf bank_mask:0xf bound_ctrl:1
	s_nop 0
	v_mfma_f32_16x16x32_f16 v[144:147], v[26:29], v[124:127], v[74:77]
	v_mfma_f32_16x16x32_f16 v[132:135], v[6:9], v[128:131], v[132:135]
	v_fma_f32 v154, v106, v150, v108
	v_fma_f32 v155, v107, v151, v109
	v_mfma_f32_16x16x32_f16 v[136:139], v[14:17], v[128:131], v[136:139]
	v_fma_f32 v152, v102, v148, v104
	v_fma_f32 v153, v103, v149, v105
	v_mfma_f32_16x16x32_f16 v[140:143], v[22:25], v[128:131], v[140:143]
	ds_write_b32 v164, v124 offset:3168
	ds_write_b32 v164, v128 offset:3172
	v_mfma_f32_16x16x32_f16 v[144:147], v[30:33], v[128:131], v[144:147]
	global_load_dwordx4 v[74:77], v[0:1], off offset:-256
	s_nop 0
	v_cndmask_b32_e64 v160, v136, v132, s[0:1]
	v_cndmask_b32_e64 v161, v137, v133, s[0:1]
	v_cndmask_b32_e64 v162, v138, v134, s[0:1]
	v_cndmask_b32_e64 v163, v139, v135, s[0:1]
	v_cndmask_b32_e64 v160, v140, v160, s[2:3]
	v_cndmask_b32_e64 v161, v141, v161, s[2:3]
	v_cndmask_b32_e64 v162, v142, v162, s[2:3]
	v_cndmask_b32_e64 v163, v143, v163, s[2:3]
	v_cndmask_b32_e64 v156, v160, v144, s[4:5]
	v_cndmask_b32_e64 v157, v161, v145, s[4:5]
	v_exp_f32_e32 v156, v156
	v_exp_f32_e32 v157, v157
	v_cndmask_b32_e64 v158, v162, v146, s[4:5]
	v_cndmask_b32_e64 v159, v163, v147, s[4:5]
	v_pk_add_f32 v[156:157], v[156:157], 1.0 op_sel_hi:[1,0]
	v_exp_f32_e32 v158, v158
	v_rcp_f32_e32 v156, v156
	v_rcp_f32_e32 v157, v157
	v_exp_f32_e32 v159, v159
	v_pk_fma_f32 v[148:149], v[110:111], v[156:157], v[152:153]
	v_pk_add_f32 v[158:159], v[158:159], 1.0 op_sel_hi:[1,0]
	v_cvt_pk_f16_f32 v124, v148, v149
	v_rcp_f32_e32 v158, v158
	v_rcp_f32_e32 v159, v159
	v_mov_b32_dpp v125, v124 quad_perm:[1,2,3,0] row_mask:0xf bank_mask:0xf bound_ctrl:1
	v_mov_b32_dpp v126, v124 quad_perm:[2,3,0,1] row_mask:0xf bank_mask:0xf bound_ctrl:1
	v_mov_b32_dpp v127, v124 quad_perm:[3,0,1,2] row_mask:0xf bank_mask:0xf bound_ctrl:1
	v_pk_fma_f32 v[150:151], v[112:113], v[158:159], v[154:155]
	s_waitcnt vmcnt(15)
	v_mfma_f32_16x16x32_f16 v[132:135], v[2:5], v[124:127], v[66:69]
	v_cvt_pk_f16_f32 v128, v150, v151
	s_nop 0
	v_mfma_f32_16x16x32_f16 v[136:139], v[10:13], v[124:127], v[66:69]
	v_mov_b32_dpp v129, v128 quad_perm:[1,2,3,0] row_mask:0xf bank_mask:0xf bound_ctrl:1
	v_mov_b32_dpp v130, v128 quad_perm:[2,3,0,1] row_mask:0xf bank_mask:0xf bound_ctrl:1
	v_mfma_f32_16x16x32_f16 v[140:143], v[18:21], v[124:127], v[66:69]
	v_mov_b32_dpp v131, v128 quad_perm:[3,0,1,2] row_mask:0xf bank_mask:0xf bound_ctrl:1
	s_nop 0
	v_mfma_f32_16x16x32_f16 v[144:147], v[26:29], v[124:127], v[66:69]
	v_mfma_f32_16x16x32_f16 v[132:135], v[6:9], v[128:131], v[132:135]
	v_fma_f32 v154, v106, v150, v108
	v_fma_f32 v155, v107, v151, v109
	v_mfma_f32_16x16x32_f16 v[136:139], v[14:17], v[128:131], v[136:139]
	v_fma_f32 v152, v102, v148, v104
	v_fma_f32 v153, v103, v149, v105
	v_mfma_f32_16x16x32_f16 v[140:143], v[22:25], v[128:131], v[140:143]
	ds_write_b32 v164, v124 offset:3696
	ds_write_b32 v164, v128 offset:3700
	v_mfma_f32_16x16x32_f16 v[144:147], v[30:33], v[128:131], v[144:147]
	global_load_dwordx4 v[66:69], v[0:1], off offset:0
	s_nop 0
	v_cndmask_b32_e64 v160, v136, v132, s[0:1]
	v_cndmask_b32_e64 v161, v137, v133, s[0:1]
	v_cndmask_b32_e64 v162, v138, v134, s[0:1]
	v_cndmask_b32_e64 v163, v139, v135, s[0:1]
	v_cndmask_b32_e64 v160, v140, v160, s[2:3]
	v_cndmask_b32_e64 v161, v141, v161, s[2:3]
	v_cndmask_b32_e64 v162, v142, v162, s[2:3]
	v_cndmask_b32_e64 v163, v143, v163, s[2:3]
	v_cndmask_b32_e64 v156, v160, v144, s[4:5]
	v_cndmask_b32_e64 v157, v161, v145, s[4:5]
	v_exp_f32_e32 v156, v156
	v_exp_f32_e32 v157, v157
	v_cndmask_b32_e64 v158, v162, v146, s[4:5]
	v_cndmask_b32_e64 v159, v163, v147, s[4:5]
	v_pk_add_f32 v[156:157], v[156:157], 1.0 op_sel_hi:[1,0]
	v_exp_f32_e32 v158, v158
	v_rcp_f32_e32 v156, v156
	v_rcp_f32_e32 v157, v157
	v_exp_f32_e32 v159, v159
	v_pk_fma_f32 v[148:149], v[110:111], v[156:157], v[152:153]
	v_pk_add_f32 v[158:159], v[158:159], 1.0 op_sel_hi:[1,0]
	v_cvt_pk_f16_f32 v124, v148, v149
	v_rcp_f32_e32 v158, v158
	v_rcp_f32_e32 v159, v159
	v_mov_b32_dpp v125, v124 quad_perm:[1,2,3,0] row_mask:0xf bank_mask:0xf bound_ctrl:1
	v_mov_b32_dpp v126, v124 quad_perm:[2,3,0,1] row_mask:0xf bank_mask:0xf bound_ctrl:1
	v_mov_b32_dpp v127, v124 quad_perm:[3,0,1,2] row_mask:0xf bank_mask:0xf bound_ctrl:1
	v_pk_fma_f32 v[150:151], v[112:113], v[158:159], v[154:155]
	s_waitcnt vmcnt(15)
	v_mfma_f32_16x16x32_f16 v[132:135], v[2:5], v[124:127], v[58:61]
	v_cvt_pk_f16_f32 v128, v150, v151
	s_nop 0
	v_mfma_f32_16x16x32_f16 v[136:139], v[10:13], v[124:127], v[58:61]
	v_mov_b32_dpp v129, v128 quad_perm:[1,2,3,0] row_mask:0xf bank_mask:0xf bound_ctrl:1
	v_mov_b32_dpp v130, v128 quad_perm:[2,3,0,1] row_mask:0xf bank_mask:0xf bound_ctrl:1
	v_mfma_f32_16x16x32_f16 v[140:143], v[18:21], v[124:127], v[58:61]
	v_mov_b32_dpp v131, v128 quad_perm:[3,0,1,2] row_mask:0xf bank_mask:0xf bound_ctrl:1
	s_nop 0
	v_mfma_f32_16x16x32_f16 v[144:147], v[26:29], v[124:127], v[58:61]
	v_mfma_f32_16x16x32_f16 v[132:135], v[6:9], v[128:131], v[132:135]
	v_fma_f32 v154, v106, v150, v108
	v_fma_f32 v155, v107, v151, v109
	v_mfma_f32_16x16x32_f16 v[136:139], v[14:17], v[128:131], v[136:139]
	v_fma_f32 v152, v102, v148, v104
	v_fma_f32 v153, v103, v149, v105
	v_mfma_f32_16x16x32_f16 v[140:143], v[22:25], v[128:131], v[140:143]
	ds_write_b32 v164, v124 offset:4224
	ds_write_b32 v164, v128 offset:4228
	v_mfma_f32_16x16x32_f16 v[144:147], v[30:33], v[128:131], v[144:147]
	global_load_dwordx4 v[58:61], v[0:1], off offset:256
	s_nop 0
	v_cndmask_b32_e64 v160, v136, v132, s[0:1]
	v_cndmask_b32_e64 v161, v137, v133, s[0:1]
	v_cndmask_b32_e64 v162, v138, v134, s[0:1]
	v_cndmask_b32_e64 v163, v139, v135, s[0:1]
	v_cndmask_b32_e64 v160, v140, v160, s[2:3]
	v_cndmask_b32_e64 v161, v141, v161, s[2:3]
	v_cndmask_b32_e64 v162, v142, v162, s[2:3]
	v_cndmask_b32_e64 v163, v143, v163, s[2:3]
	v_cndmask_b32_e64 v156, v160, v144, s[4:5]
	v_cndmask_b32_e64 v157, v161, v145, s[4:5]
	v_exp_f32_e32 v156, v156
	v_exp_f32_e32 v157, v157
	v_cndmask_b32_e64 v158, v162, v146, s[4:5]
	v_cndmask_b32_e64 v159, v163, v147, s[4:5]
	v_pk_add_f32 v[156:157], v[156:157], 1.0 op_sel_hi:[1,0]
	v_exp_f32_e32 v158, v158
	v_rcp_f32_e32 v156, v156
	v_rcp_f32_e32 v157, v157
	v_exp_f32_e32 v159, v159
	v_pk_fma_f32 v[148:149], v[110:111], v[156:157], v[152:153]
	v_pk_add_f32 v[158:159], v[158:159], 1.0 op_sel_hi:[1,0]
	v_cvt_pk_f16_f32 v124, v148, v149
	v_rcp_f32_e32 v158, v158
	v_rcp_f32_e32 v159, v159
	v_mov_b32_dpp v125, v124 quad_perm:[1,2,3,0] row_mask:0xf bank_mask:0xf bound_ctrl:1
	v_mov_b32_dpp v126, v124 quad_perm:[2,3,0,1] row_mask:0xf bank_mask:0xf bound_ctrl:1
	v_mov_b32_dpp v127, v124 quad_perm:[3,0,1,2] row_mask:0xf bank_mask:0xf bound_ctrl:1
	v_pk_fma_f32 v[150:151], v[112:113], v[158:159], v[154:155]
	s_waitcnt vmcnt(15)
	v_mfma_f32_16x16x32_f16 v[132:135], v[2:5], v[124:127], v[54:57]
	v_cvt_pk_f16_f32 v128, v150, v151
	s_nop 0
	v_mfma_f32_16x16x32_f16 v[136:139], v[10:13], v[124:127], v[54:57]
	v_mov_b32_dpp v129, v128 quad_perm:[1,2,3,0] row_mask:0xf bank_mask:0xf bound_ctrl:1
	v_mov_b32_dpp v130, v128 quad_perm:[2,3,0,1] row_mask:0xf bank_mask:0xf bound_ctrl:1
	v_mfma_f32_16x16x32_f16 v[140:143], v[18:21], v[124:127], v[54:57]
	v_mov_b32_dpp v131, v128 quad_perm:[3,0,1,2] row_mask:0xf bank_mask:0xf bound_ctrl:1
	s_nop 0
	v_mfma_f32_16x16x32_f16 v[144:147], v[26:29], v[124:127], v[54:57]
	v_mfma_f32_16x16x32_f16 v[132:135], v[6:9], v[128:131], v[132:135]
	v_fma_f32 v154, v106, v150, v108
	v_fma_f32 v155, v107, v151, v109
	v_mfma_f32_16x16x32_f16 v[136:139], v[14:17], v[128:131], v[136:139]
	v_fma_f32 v152, v102, v148, v104
	v_fma_f32 v153, v103, v149, v105
	v_mfma_f32_16x16x32_f16 v[140:143], v[22:25], v[128:131], v[140:143]
	ds_write_b32 v164, v124 offset:4752
	ds_write_b32 v164, v128 offset:4756
	v_mfma_f32_16x16x32_f16 v[144:147], v[30:33], v[128:131], v[144:147]
	global_load_dwordx4 v[54:57], v[0:1], off offset:512
	s_nop 0
	v_cndmask_b32_e64 v160, v136, v132, s[0:1]
	v_cndmask_b32_e64 v161, v137, v133, s[0:1]
	v_cndmask_b32_e64 v162, v138, v134, s[0:1]
	v_cndmask_b32_e64 v163, v139, v135, s[0:1]
	v_cndmask_b32_e64 v160, v140, v160, s[2:3]
	v_cndmask_b32_e64 v161, v141, v161, s[2:3]
	v_cndmask_b32_e64 v162, v142, v162, s[2:3]
	v_cndmask_b32_e64 v163, v143, v163, s[2:3]
	v_cndmask_b32_e64 v156, v160, v144, s[4:5]
	v_cndmask_b32_e64 v157, v161, v145, s[4:5]
	v_exp_f32_e32 v156, v156
	v_exp_f32_e32 v157, v157
	v_cndmask_b32_e64 v158, v162, v146, s[4:5]
	v_cndmask_b32_e64 v159, v163, v147, s[4:5]
	v_pk_add_f32 v[156:157], v[156:157], 1.0 op_sel_hi:[1,0]
	v_exp_f32_e32 v158, v158
	v_rcp_f32_e32 v156, v156
	v_rcp_f32_e32 v157, v157
	v_exp_f32_e32 v159, v159
	v_pk_fma_f32 v[148:149], v[110:111], v[156:157], v[152:153]
	v_pk_add_f32 v[158:159], v[158:159], 1.0 op_sel_hi:[1,0]
	v_cvt_pk_f16_f32 v124, v148, v149
	v_rcp_f32_e32 v158, v158
	v_rcp_f32_e32 v159, v159
	v_mov_b32_dpp v125, v124 quad_perm:[1,2,3,0] row_mask:0xf bank_mask:0xf bound_ctrl:1
	v_mov_b32_dpp v126, v124 quad_perm:[2,3,0,1] row_mask:0xf bank_mask:0xf bound_ctrl:1
	v_mov_b32_dpp v127, v124 quad_perm:[3,0,1,2] row_mask:0xf bank_mask:0xf bound_ctrl:1
	v_pk_fma_f32 v[150:151], v[112:113], v[158:159], v[154:155]
	s_waitcnt vmcnt(15)
	v_mfma_f32_16x16x32_f16 v[132:135], v[2:5], v[124:127], v[50:53]
	v_cvt_pk_f16_f32 v128, v150, v151
	s_nop 0
	v_mfma_f32_16x16x32_f16 v[136:139], v[10:13], v[124:127], v[50:53]
	v_mov_b32_dpp v129, v128 quad_perm:[1,2,3,0] row_mask:0xf bank_mask:0xf bound_ctrl:1
	v_mov_b32_dpp v130, v128 quad_perm:[2,3,0,1] row_mask:0xf bank_mask:0xf bound_ctrl:1
	v_mfma_f32_16x16x32_f16 v[140:143], v[18:21], v[124:127], v[50:53]
	v_mov_b32_dpp v131, v128 quad_perm:[3,0,1,2] row_mask:0xf bank_mask:0xf bound_ctrl:1
	s_nop 0
	v_mfma_f32_16x16x32_f16 v[144:147], v[26:29], v[124:127], v[50:53]
	v_mfma_f32_16x16x32_f16 v[132:135], v[6:9], v[128:131], v[132:135]
	v_fma_f32 v154, v106, v150, v108
	v_fma_f32 v155, v107, v151, v109
	v_mfma_f32_16x16x32_f16 v[136:139], v[14:17], v[128:131], v[136:139]
	v_fma_f32 v152, v102, v148, v104
	v_fma_f32 v153, v103, v149, v105
	v_mfma_f32_16x16x32_f16 v[140:143], v[22:25], v[128:131], v[140:143]
	ds_write_b32 v164, v124 offset:5280
	ds_write_b32 v164, v128 offset:5284
	v_mfma_f32_16x16x32_f16 v[144:147], v[30:33], v[128:131], v[144:147]
	global_load_dwordx4 v[50:53], v[0:1], off offset:768
	s_nop 0
	v_cndmask_b32_e64 v160, v136, v132, s[0:1]
	v_cndmask_b32_e64 v161, v137, v133, s[0:1]
	v_cndmask_b32_e64 v162, v138, v134, s[0:1]
	v_cndmask_b32_e64 v163, v139, v135, s[0:1]
	v_cndmask_b32_e64 v160, v140, v160, s[2:3]
	v_cndmask_b32_e64 v161, v141, v161, s[2:3]
	v_cndmask_b32_e64 v162, v142, v162, s[2:3]
	v_cndmask_b32_e64 v163, v143, v163, s[2:3]
	v_cndmask_b32_e64 v156, v160, v144, s[4:5]
	v_cndmask_b32_e64 v157, v161, v145, s[4:5]
	v_exp_f32_e32 v156, v156
	v_exp_f32_e32 v157, v157
	v_cndmask_b32_e64 v158, v162, v146, s[4:5]
	v_cndmask_b32_e64 v159, v163, v147, s[4:5]
	v_pk_add_f32 v[156:157], v[156:157], 1.0 op_sel_hi:[1,0]
	v_exp_f32_e32 v158, v158
	v_rcp_f32_e32 v156, v156
	v_rcp_f32_e32 v157, v157
	v_exp_f32_e32 v159, v159
	v_pk_fma_f32 v[148:149], v[110:111], v[156:157], v[152:153]
	v_pk_add_f32 v[158:159], v[158:159], 1.0 op_sel_hi:[1,0]
	v_cvt_pk_f16_f32 v124, v148, v149
	v_rcp_f32_e32 v158, v158
	v_rcp_f32_e32 v159, v159
	v_mov_b32_dpp v125, v124 quad_perm:[1,2,3,0] row_mask:0xf bank_mask:0xf bound_ctrl:1
	v_mov_b32_dpp v126, v124 quad_perm:[2,3,0,1] row_mask:0xf bank_mask:0xf bound_ctrl:1
	v_mov_b32_dpp v127, v124 quad_perm:[3,0,1,2] row_mask:0xf bank_mask:0xf bound_ctrl:1
	v_pk_fma_f32 v[150:151], v[112:113], v[158:159], v[154:155]
	s_waitcnt vmcnt(15)
	v_mfma_f32_16x16x32_f16 v[132:135], v[2:5], v[124:127], v[46:49]
	v_cvt_pk_f16_f32 v128, v150, v151
	s_nop 0
	v_mfma_f32_16x16x32_f16 v[136:139], v[10:13], v[124:127], v[46:49]
	v_mov_b32_dpp v129, v128 quad_perm:[1,2,3,0] row_mask:0xf bank_mask:0xf bound_ctrl:1
	v_mov_b32_dpp v130, v128 quad_perm:[2,3,0,1] row_mask:0xf bank_mask:0xf bound_ctrl:1
	v_mfma_f32_16x16x32_f16 v[140:143], v[18:21], v[124:127], v[46:49]
	v_mov_b32_dpp v131, v128 quad_perm:[3,0,1,2] row_mask:0xf bank_mask:0xf bound_ctrl:1
	s_nop 0
	v_mfma_f32_16x16x32_f16 v[144:147], v[26:29], v[124:127], v[46:49]
	v_mfma_f32_16x16x32_f16 v[132:135], v[6:9], v[128:131], v[132:135]
	v_fma_f32 v154, v106, v150, v108
	v_fma_f32 v155, v107, v151, v109
	v_mfma_f32_16x16x32_f16 v[136:139], v[14:17], v[128:131], v[136:139]
	v_fma_f32 v152, v102, v148, v104
	v_fma_f32 v153, v103, v149, v105
	v_mfma_f32_16x16x32_f16 v[140:143], v[22:25], v[128:131], v[140:143]
	ds_write_b32 v164, v124 offset:5808
	ds_write_b32 v164, v128 offset:5812
	v_mfma_f32_16x16x32_f16 v[144:147], v[30:33], v[128:131], v[144:147]
	global_load_dwordx4 v[46:49], v[0:1], off offset:1024
	s_nop 0
	v_cndmask_b32_e64 v160, v136, v132, s[0:1]
	v_cndmask_b32_e64 v161, v137, v133, s[0:1]
	v_cndmask_b32_e64 v162, v138, v134, s[0:1]
	v_cndmask_b32_e64 v163, v139, v135, s[0:1]
	v_cndmask_b32_e64 v160, v140, v160, s[2:3]
	v_cndmask_b32_e64 v161, v141, v161, s[2:3]
	v_cndmask_b32_e64 v162, v142, v162, s[2:3]
	v_cndmask_b32_e64 v163, v143, v163, s[2:3]
	v_cndmask_b32_e64 v156, v160, v144, s[4:5]
	v_cndmask_b32_e64 v157, v161, v145, s[4:5]
	v_exp_f32_e32 v156, v156
	v_exp_f32_e32 v157, v157
	v_cndmask_b32_e64 v158, v162, v146, s[4:5]
	v_cndmask_b32_e64 v159, v163, v147, s[4:5]
	v_pk_add_f32 v[156:157], v[156:157], 1.0 op_sel_hi:[1,0]
	v_exp_f32_e32 v158, v158
	v_rcp_f32_e32 v156, v156
	v_rcp_f32_e32 v157, v157
	v_exp_f32_e32 v159, v159
	v_pk_fma_f32 v[148:149], v[110:111], v[156:157], v[152:153]
	v_pk_add_f32 v[158:159], v[158:159], 1.0 op_sel_hi:[1,0]
	v_cvt_pk_f16_f32 v124, v148, v149
	v_rcp_f32_e32 v158, v158
	v_rcp_f32_e32 v159, v159
	v_mov_b32_dpp v125, v124 quad_perm:[1,2,3,0] row_mask:0xf bank_mask:0xf bound_ctrl:1
	v_mov_b32_dpp v126, v124 quad_perm:[2,3,0,1] row_mask:0xf bank_mask:0xf bound_ctrl:1
	v_mov_b32_dpp v127, v124 quad_perm:[3,0,1,2] row_mask:0xf bank_mask:0xf bound_ctrl:1
	v_pk_fma_f32 v[150:151], v[112:113], v[158:159], v[154:155]
	s_waitcnt vmcnt(15)
	v_mfma_f32_16x16x32_f16 v[132:135], v[2:5], v[124:127], v[42:45]
	v_cvt_pk_f16_f32 v128, v150, v151
	s_nop 0
	v_mfma_f32_16x16x32_f16 v[136:139], v[10:13], v[124:127], v[42:45]
	v_mov_b32_dpp v129, v128 quad_perm:[1,2,3,0] row_mask:0xf bank_mask:0xf bound_ctrl:1
	v_mov_b32_dpp v130, v128 quad_perm:[2,3,0,1] row_mask:0xf bank_mask:0xf bound_ctrl:1
	v_mfma_f32_16x16x32_f16 v[140:143], v[18:21], v[124:127], v[42:45]
	v_mov_b32_dpp v131, v128 quad_perm:[3,0,1,2] row_mask:0xf bank_mask:0xf bound_ctrl:1
	s_nop 0
	v_mfma_f32_16x16x32_f16 v[144:147], v[26:29], v[124:127], v[42:45]
	v_mfma_f32_16x16x32_f16 v[132:135], v[6:9], v[128:131], v[132:135]
	v_fma_f32 v154, v106, v150, v108
	v_fma_f32 v155, v107, v151, v109
	v_mfma_f32_16x16x32_f16 v[136:139], v[14:17], v[128:131], v[136:139]
	v_fma_f32 v152, v102, v148, v104
	v_fma_f32 v153, v103, v149, v105
	v_mfma_f32_16x16x32_f16 v[140:143], v[22:25], v[128:131], v[140:143]
	ds_write_b32 v164, v124 offset:6336
	ds_write_b32 v164, v128 offset:6340
	v_mfma_f32_16x16x32_f16 v[144:147], v[30:33], v[128:131], v[144:147]
	global_load_dwordx4 v[42:45], v[0:1], off offset:1280
	s_nop 0
	v_cndmask_b32_e64 v160, v136, v132, s[0:1]
	v_cndmask_b32_e64 v161, v137, v133, s[0:1]
	v_cndmask_b32_e64 v162, v138, v134, s[0:1]
	v_cndmask_b32_e64 v163, v139, v135, s[0:1]
	v_cndmask_b32_e64 v160, v140, v160, s[2:3]
	v_cndmask_b32_e64 v161, v141, v161, s[2:3]
	v_cndmask_b32_e64 v162, v142, v162, s[2:3]
	v_cndmask_b32_e64 v163, v143, v163, s[2:3]
	v_cndmask_b32_e64 v156, v160, v144, s[4:5]
	v_cndmask_b32_e64 v157, v161, v145, s[4:5]
	v_exp_f32_e32 v156, v156
	v_exp_f32_e32 v157, v157
	v_cndmask_b32_e64 v158, v162, v146, s[4:5]
	v_cndmask_b32_e64 v159, v163, v147, s[4:5]
	v_pk_add_f32 v[156:157], v[156:157], 1.0 op_sel_hi:[1,0]
	v_exp_f32_e32 v158, v158
	v_rcp_f32_e32 v156, v156
	v_rcp_f32_e32 v157, v157
	v_exp_f32_e32 v159, v159
	v_pk_fma_f32 v[148:149], v[110:111], v[156:157], v[152:153]
	v_pk_add_f32 v[158:159], v[158:159], 1.0 op_sel_hi:[1,0]
	v_cvt_pk_f16_f32 v124, v148, v149
	v_rcp_f32_e32 v158, v158
	v_rcp_f32_e32 v159, v159
	v_mov_b32_dpp v125, v124 quad_perm:[1,2,3,0] row_mask:0xf bank_mask:0xf bound_ctrl:1
	v_mov_b32_dpp v126, v124 quad_perm:[2,3,0,1] row_mask:0xf bank_mask:0xf bound_ctrl:1
	v_mov_b32_dpp v127, v124 quad_perm:[3,0,1,2] row_mask:0xf bank_mask:0xf bound_ctrl:1
	v_pk_fma_f32 v[150:151], v[112:113], v[158:159], v[154:155]
	s_waitcnt vmcnt(15)
	v_mfma_f32_16x16x32_f16 v[132:135], v[2:5], v[124:127], v[38:41]
	v_cvt_pk_f16_f32 v128, v150, v151
	s_nop 0
	v_mfma_f32_16x16x32_f16 v[136:139], v[10:13], v[124:127], v[38:41]
	v_mov_b32_dpp v129, v128 quad_perm:[1,2,3,0] row_mask:0xf bank_mask:0xf bound_ctrl:1
	v_mov_b32_dpp v130, v128 quad_perm:[2,3,0,1] row_mask:0xf bank_mask:0xf bound_ctrl:1
	v_mfma_f32_16x16x32_f16 v[140:143], v[18:21], v[124:127], v[38:41]
	v_mov_b32_dpp v131, v128 quad_perm:[3,0,1,2] row_mask:0xf bank_mask:0xf bound_ctrl:1
	s_nop 0
	v_mfma_f32_16x16x32_f16 v[144:147], v[26:29], v[124:127], v[38:41]
	v_mfma_f32_16x16x32_f16 v[132:135], v[6:9], v[128:131], v[132:135]
	v_fma_f32 v154, v106, v150, v108
	v_fma_f32 v155, v107, v151, v109
	v_mfma_f32_16x16x32_f16 v[136:139], v[14:17], v[128:131], v[136:139]
	v_fma_f32 v152, v102, v148, v104
	v_fma_f32 v153, v103, v149, v105
	v_mfma_f32_16x16x32_f16 v[140:143], v[22:25], v[128:131], v[140:143]
	ds_write_b32 v164, v124 offset:6864
	ds_write_b32 v164, v128 offset:6868
	v_mfma_f32_16x16x32_f16 v[144:147], v[30:33], v[128:131], v[144:147]
	global_load_dwordx4 v[38:41], v[0:1], off offset:1536
	s_nop 0
	v_cndmask_b32_e64 v160, v136, v132, s[0:1]
	v_cndmask_b32_e64 v161, v137, v133, s[0:1]
	v_cndmask_b32_e64 v162, v138, v134, s[0:1]
	v_cndmask_b32_e64 v163, v139, v135, s[0:1]
	v_cndmask_b32_e64 v160, v140, v160, s[2:3]
	v_cndmask_b32_e64 v161, v141, v161, s[2:3]
	v_cndmask_b32_e64 v162, v142, v162, s[2:3]
	v_cndmask_b32_e64 v163, v143, v163, s[2:3]
	v_cndmask_b32_e64 v156, v160, v144, s[4:5]
	v_cndmask_b32_e64 v157, v161, v145, s[4:5]
	v_exp_f32_e32 v156, v156
	v_exp_f32_e32 v157, v157
	v_cndmask_b32_e64 v158, v162, v146, s[4:5]
	v_cndmask_b32_e64 v159, v163, v147, s[4:5]
	v_pk_add_f32 v[156:157], v[156:157], 1.0 op_sel_hi:[1,0]
	v_exp_f32_e32 v158, v158
	v_rcp_f32_e32 v156, v156
	v_rcp_f32_e32 v157, v157
	v_exp_f32_e32 v159, v159
	v_pk_fma_f32 v[148:149], v[110:111], v[156:157], v[152:153]
	v_pk_add_f32 v[158:159], v[158:159], 1.0 op_sel_hi:[1,0]
	v_cvt_pk_f16_f32 v124, v148, v149
	v_rcp_f32_e32 v158, v158
	v_rcp_f32_e32 v159, v159
	v_mov_b32_dpp v125, v124 quad_perm:[1,2,3,0] row_mask:0xf bank_mask:0xf bound_ctrl:1
	v_mov_b32_dpp v126, v124 quad_perm:[2,3,0,1] row_mask:0xf bank_mask:0xf bound_ctrl:1
	v_mov_b32_dpp v127, v124 quad_perm:[3,0,1,2] row_mask:0xf bank_mask:0xf bound_ctrl:1
	v_pk_fma_f32 v[150:151], v[112:113], v[158:159], v[154:155]
	s_waitcnt vmcnt(15)
	v_mfma_f32_16x16x32_f16 v[132:135], v[2:5], v[124:127], v[34:37]
	v_cvt_pk_f16_f32 v128, v150, v151
	s_nop 0
	v_mfma_f32_16x16x32_f16 v[136:139], v[10:13], v[124:127], v[34:37]
	v_mov_b32_dpp v129, v128 quad_perm:[1,2,3,0] row_mask:0xf bank_mask:0xf bound_ctrl:1
	v_mov_b32_dpp v130, v128 quad_perm:[2,3,0,1] row_mask:0xf bank_mask:0xf bound_ctrl:1
	v_mfma_f32_16x16x32_f16 v[140:143], v[18:21], v[124:127], v[34:37]
	v_mov_b32_dpp v131, v128 quad_perm:[3,0,1,2] row_mask:0xf bank_mask:0xf bound_ctrl:1
	s_nop 0
	v_mfma_f32_16x16x32_f16 v[144:147], v[26:29], v[124:127], v[34:37]
	v_mfma_f32_16x16x32_f16 v[132:135], v[6:9], v[128:131], v[132:135]
	v_fma_f32 v154, v106, v150, v108
	v_fma_f32 v155, v107, v151, v109
	v_mfma_f32_16x16x32_f16 v[136:139], v[14:17], v[128:131], v[136:139]
	v_fma_f32 v152, v102, v148, v104
	v_fma_f32 v153, v103, v149, v105
	v_mfma_f32_16x16x32_f16 v[140:143], v[22:25], v[128:131], v[140:143]
	ds_write_b32 v164, v124 offset:7392
	ds_write_b32 v164, v128 offset:7396
	v_mfma_f32_16x16x32_f16 v[144:147], v[30:33], v[128:131], v[144:147]
	global_load_dwordx4 v[34:37], v[0:1], off offset:1792
	s_nop 0
	v_cndmask_b32_e64 v160, v136, v132, s[0:1]
	v_cndmask_b32_e64 v161, v137, v133, s[0:1]
	v_cndmask_b32_e64 v162, v138, v134, s[0:1]
	v_cndmask_b32_e64 v163, v139, v135, s[0:1]
	v_cndmask_b32_e64 v160, v140, v160, s[2:3]
	v_cndmask_b32_e64 v161, v141, v161, s[2:3]
	v_cndmask_b32_e64 v162, v142, v162, s[2:3]
	v_cndmask_b32_e64 v163, v143, v163, s[2:3]
	v_cndmask_b32_e64 v156, v160, v144, s[4:5]
	v_cndmask_b32_e64 v157, v161, v145, s[4:5]
	v_exp_f32_e32 v156, v156
	v_exp_f32_e32 v157, v157
	v_cndmask_b32_e64 v158, v162, v146, s[4:5]
	v_cndmask_b32_e64 v159, v163, v147, s[4:5]
	v_pk_add_f32 v[156:157], v[156:157], 1.0 op_sel_hi:[1,0]
	v_exp_f32_e32 v158, v158
	v_rcp_f32_e32 v156, v156
	v_rcp_f32_e32 v157, v157
	v_exp_f32_e32 v159, v159
	v_pk_fma_f32 v[148:149], v[110:111], v[156:157], v[152:153]
	v_pk_add_f32 v[158:159], v[158:159], 1.0 op_sel_hi:[1,0]
	v_cvt_pk_f16_f32 v124, v148, v149
	v_rcp_f32_e32 v158, v158
	v_rcp_f32_e32 v159, v159
	v_mov_b32_dpp v125, v124 quad_perm:[1,2,3,0] row_mask:0xf bank_mask:0xf bound_ctrl:1
	v_mov_b32_dpp v126, v124 quad_perm:[2,3,0,1] row_mask:0xf bank_mask:0xf bound_ctrl:1
	v_mov_b32_dpp v127, v124 quad_perm:[3,0,1,2] row_mask:0xf bank_mask:0xf bound_ctrl:1
	v_pk_fma_f32 v[150:151], v[112:113], v[158:159], v[154:155]
	s_nop 0
	v_cvt_pk_f16_f32 v128, v150, v151
	ds_write_b32 v164, v124 offset:7920
	v_fma_f32 v152, v102, v148, v104
	v_mov_b32_dpp v129, v128 quad_perm:[1,2,3,0] row_mask:0xf bank_mask:0xf bound_ctrl:1
	v_mov_b32_dpp v130, v128 quad_perm:[2,3,0,1] row_mask:0xf bank_mask:0xf bound_ctrl:1
	v_mov_b32_dpp v131, v128 quad_perm:[3,0,1,2] row_mask:0xf bank_mask:0xf bound_ctrl:1
	ds_write_b32 v164, v128 offset:7924
	v_fma_f32 v153, v103, v149, v105
	v_fma_f32 v154, v106, v150, v108
	v_fma_f32 v155, v107, v151, v109
	s_branch .LBB3_168
